# N2 image-build loads issued up front; N1 row tail: next-row/inv wait moved after the row-norm reduction as a counted wait
# speedup vs baseline: 1.0283x; 1.0025x over previous
.LBB0_221:
	v_pk_mul_f32 v[4:5], v[34:35], v[34:35]
	v_pk_mul_f32 v[6:7], v[32:33], v[32:33]
	v_pk_mul_f32 v[0:1], v[38:39], v[38:39]
	s_waitcnt lgkmcnt(0)
	v_pk_mul_f32 v[2:3], v[36:37], v[36:37]
	v_pk_mov_b32 v[8:9], v[6:7], v[4:5] op_sel:[1,0]
	v_mov_b32_e32 v7, v5
	v_pk_add_f32 v[4:5], v[8:9], v[6:7]
	v_pk_mov_b32 v[6:7], v[2:3], v[0:1] op_sel:[1,0]
	v_mov_b32_e32 v3, v1
	v_pk_add_f32 v[0:1], v[6:7], v[2:3]
	v_pk_add_f32 v[4:5], v[4:5], v[4:5] op_sel_hi:[0,1]
	v_pk_add_f32 v[0:1], v[0:1], v[0:1] op_sel_hi:[0,1]
	v_mul_f32_e32 v0, v40, v40
	v_pk_fma_f32 v[2:3], v[40:41], v[40:41], v[0:1] op_sel_hi:[1,1,0]
	v_mul_f32_e32 v0, v42, v42
	v_pk_fma_f32 v[6:7], v[42:43], v[42:43], v[0:1] op_sel_hi:[1,1,0]
	v_mul_f32_e32 v2, v28, v28
	v_mul_f32_e32 v6, v29, v29
	v_mul_f32_e32 v4, v30, v30
	v_mul_f32_e32 v0, v31, v31
	v_pk_add_f32 v[2:3], v[2:3], v[6:7]
	v_pk_add_f32 v[0:1], v[4:5], v[0:1]
	s_andn2_b64 vcc, exec, s[14:15]
	v_pk_add_f32 v[0:1], v[2:3], v[0:1]
	v_lshl_add_u64 v[2:3], v[120:121], 0, s[16:17]
	v_add_f32_e32 v0, v0, v1
	ds_bpermute_b32 v1, v129, v0
	s_mov_b32 s10, s12
	s_waitcnt lgkmcnt(0)
	v_add_f32_e32 v0, v0, v1
	ds_bpermute_b32 v1, v130, v0
	s_waitcnt lgkmcnt(0)
	v_add_f32_e32 v0, v0, v1
	ds_bpermute_b32 v1, v131, v0
	s_waitcnt lgkmcnt(0)
	v_add_f32_e32 v0, v0, v1
	ds_bpermute_b32 v1, v132, v0
	s_waitcnt lgkmcnt(0)
	v_add_f32_e32 v0, v0, v1
	ds_bpermute_b32 v1, v133, v0
	s_waitcnt lgkmcnt(0)
	v_add_f32_e32 v0, v0, v1
	ds_bpermute_b32 v1, v134, v0
	s_waitcnt lgkmcnt(0)
	v_add_f32_e32 v0, v0, v1
	v_fmamk_f32 v0, v0, 0x3a800000, v200
	v_rsq_f32_e32 v0, v0
	s_nop 0
	v_pk_mul_f32 v[4:5], v[32:33], v[0:1] op_sel_hi:[1,0]
	v_pk_mul_f32 v[6:7], v[34:35], v[0:1] op_sel_hi:[1,0]
	v_pk_fma_f32 v[4:5], v[82:83], v[4:5], v[60:61]
	v_pk_mul_f32 v[8:9], v[36:37], v[0:1] op_sel_hi:[1,0]
	v_pk_mul_f32 v[10:11], v[38:39], v[0:1] op_sel_hi:[1,0]
	v_pk_fma_f32 v[6:7], v[84:85], v[6:7], v[62:63]
	v_cvt_pk_bf16_f32 v4, v4, v5
	v_pk_fma_f32 v[10:11], v[88:89], v[10:11], v[72:73]
	v_cvt_pk_bf16_f32 v5, v6, v7
	v_pk_fma_f32 v[8:9], v[86:87], v[8:9], v[70:71]
	global_store_dwordx2 v[2:3], v[4:5], off
	v_cvt_pk_bf16_f32 v4, v8, v9
	v_cvt_pk_bf16_f32 v5, v10, v11
	v_pk_mul_f32 v[12:13], v[40:41], v[0:1] op_sel_hi:[1,0]
	global_store_dwordx2 v[2:3], v[4:5], off offset:512
	v_pk_mul_f32 v[4:5], v[42:43], v[0:1] op_sel_hi:[1,0]
	v_pk_fma_f32 v[6:7], v[90:91], v[12:13], v[74:75]
	v_pk_fma_f32 v[4:5], v[92:93], v[4:5], v[76:77]
	v_cvt_pk_bf16_f32 v6, v6, v7
	v_cvt_pk_bf16_f32 v7, v4, v5
	v_pk_mul_f32 v[4:5], v[44:45], v[0:1] op_sel_hi:[1,0]
	v_pk_mul_f32 v[0:1], v[46:47], v[0:1] op_sel_hi:[1,0]
	v_pk_fma_f32 v[4:5], v[94:95], v[4:5], v[78:79]
	global_store_dwordx2 v[2:3], v[6:7], off offset:1024
	v_pk_fma_f32 v[0:1], v[96:97], v[0:1], v[80:81]
	v_cvt_pk_bf16_f32 v4, v4, v5
	v_cvt_pk_bf16_f32 v5, v0, v1
	global_store_dwordx2 v[2:3], v[4:5], off offset:1536
	s_waitcnt vmcnt(4)
	v_mov_b32_e32 v135, v136
	v_mov_b32_e32 v14, v112
	v_mov_b32_e32 v15, v113
	v_mov_b32_e32 v8, v106
	v_mov_b32_e32 v6, v104
	v_mov_b32_e32 v0, v98
	v_mov_b32_e32 v1, v99
	v_mov_b32_e32 v2, v100
	v_mov_b32_e32 v3, v101
	v_mov_b32_e32 v4, v102
	v_mov_b32_e32 v5, v103
	v_mov_b32_e32 v7, v105
	v_mov_b32_e32 v9, v107
	v_mov_b32_e32 v10, v108
	v_mov_b32_e32 v11, v109
	v_mov_b32_e32 v12, v110
	v_mov_b32_e32 v13, v111
	s_cbranch_vccz .LBB0_245

.LBB0_979:
	v_ashrrev_i32_e32 v145, 1, v64
	s_movk_i32 s31, 0xffc0
	v_and_or_b32 v146, v145, s31, v169
	v_ashrrev_i32_e32 v147, 31, v146
	v_lshlrev_b64 v[172:173], 2, v[146:147]
	v_lshl_or_b32 v146, v146, 4, v130
	v_ashrrev_i32_e32 v147, 31, v146
	v_lshl_add_u64 v[184:185], s[20:21], 0, v[172:173]
	v_lshl_add_u64 v[190:191], v[146:147], 2, s[14:15]
	v_lshl_add_u64 v[186:187], s[18:19], 0, v[172:173]
	v_lshl_add_u64 v[188:189], s[16:17], 0, v[172:173]
	global_load_dwordx4 v[172:175], v[184:185], off
	global_load_dwordx4 v[176:179], v[186:187], off
	global_load_dwordx4 v[180:183], v[188:189], off
	global_load_dword v146, v[190:191], off
	global_load_dword v147, v[190:191], off offset:64
	global_load_dword v192, v[190:191], off offset:128
	global_load_dword v194, v[190:191], off offset:192
	global_load_dwordx4 v[222:225], v[184:185], off offset:16
	global_load_dwordx4 v[226:229], v[186:187], off offset:16
	global_load_dwordx4 v[230:233], v[188:189], off offset:16
	global_load_dword v193, v[190:191], off offset:256
	global_load_dword v195, v[190:191], off offset:320
	global_load_dword v234, v[190:191], off offset:384
	global_load_dword v235, v[190:191], off offset:448
	v_add_u32_e32 v64, 0x200, v64
	s_waitcnt vmcnt(12)
	v_pk_add_f32 v[176:177], v[176:177], 1.0 op_sel_hi:[1,0]
	s_nop 0
	v_pk_mul_f32 v[176:177], v[172:173], v[176:177]
	s_waitcnt vmcnt(9)
	v_pk_mul_f32 v[172:173], v[180:181], v[146:147]
	v_mul_f32_e32 v145, v146, v176
	v_add_f32_e32 v172, v172, v173
	v_mul_f32_e32 v171, v177, v147
	v_add_f32_e32 v211, v144, v172
	v_cvt_pk_bf16_f32 v172, v145, v171
	v_pk_add_f32 v[178:179], v[178:179], 1.0 op_sel_hi:[1,0]
	v_lshlrev_b32_e32 v144, 16, v172
	v_and_b32_e32 v145, 0xffff0000, v172
	v_fma_f32 v144, v146, v176, -v144
	v_fma_f32 v145, v177, v147, -v145
	v_cvt_pk_bf16_f32 v176, v144, v145
	v_pk_mul_f32 v[174:175], v[174:175], v[178:179]
	s_waitcnt vmcnt(8)
	v_mul_f32_e32 v144, v174, v192
	s_waitcnt vmcnt(7)
	v_mul_f32_e32 v145, v175, v194
	v_cvt_pk_bf16_f32 v173, v144, v145
	s_nop 0
	v_lshlrev_b32_e32 v144, 16, v173
	v_and_b32_e32 v145, 0xffff0000, v173
	v_fma_f32 v144, v174, v192, -v144
	v_fma_f32 v145, v175, v194, -v145
	v_cvt_pk_bf16_f32 v177, v144, v145
	s_waitcnt vmcnt(5)
	v_pk_add_f32 v[174:175], v[228:229], 1.0 op_sel_hi:[1,0]
	v_pk_add_f32 v[178:179], v[226:227], 1.0 op_sel_hi:[1,0]
	v_pk_mul_f32 v[146:147], v[224:225], v[174:175]
	s_waitcnt vmcnt(4)
	v_mov_b32_e32 v175, v230
	v_mov_b32_e32 v184, v183
	v_mov_b32_e32 v185, v231
	v_pk_mul_f32 v[144:145], v[222:223], v[178:179]
	v_mov_b32_e32 v174, v182
	s_waitcnt vmcnt(2)
	v_pk_mul_f32 v[178:179], v[184:185], v[194:195]
	v_mul_f32_e32 v171, v193, v144
	v_pk_fma_f32 v[174:175], v[174:175], v[192:193], v[178:179]
	v_mul_f32_e32 v180, v145, v195
	v_add_f32_e32 v174, v211, v174
	v_add_f32_e32 v175, v174, v175
	v_cvt_pk_bf16_f32 v174, v171, v180
	s_nop 0
	v_lshlrev_b32_e32 v171, 16, v174
	v_fma_f32 v144, v193, v144, -v171
	v_and_b32_e32 v171, 0xffff0000, v174
	v_fma_f32 v145, v145, v195, -v171
	v_cvt_pk_bf16_f32 v178, v144, v145
	s_waitcnt vmcnt(1)
	v_mul_f32_e32 v171, v146, v234
	s_waitcnt vmcnt(0)
	v_pk_mul_f32 v[144:145], v[232:233], v[234:235]
	v_mul_f32_e32 v179, v147, v235
	v_add_f32_e32 v144, v144, v145
	v_add_f32_e32 v144, v175, v144
	v_cvt_pk_bf16_f32 v175, v171, v179
	s_nop 0
	v_lshlrev_b32_e32 v145, 16, v175
	v_fma_f32 v145, v146, v234, -v145
	v_and_b32_e32 v146, 0xffff0000, v175
	v_fma_f32 v146, v147, v235, -v146
	v_cvt_pk_bf16_f32 v179, v145, v146
	v_add_u32_e32 v145, s2, v170
	s_addk_i32 s2, 0x2000
	s_cmpk_eq_u32 s2, 0x8000
	ds_write_b128 v145, v[172:175]
	ds_write_b128 v145, v[176:179] offset:32768
	s_cbranch_scc0 .LBB0_979
	ds_bpermute_b32 v64, v148, v144
	s_waitcnt lgkmcnt(0)
	v_add_f32_e32 v64, v144, v64
	ds_bpermute_b32 v144, v149, v64
	s_and_saveexec_b64 s[14:15], s[4:5]
	s_cbranch_execz .LBB0_982
	s_waitcnt lgkmcnt(0)
	v_add_f32_e32 v64, v64, v144
	ds_write_b32 v150, v64
